# cprio
# baseline (speedup 1.0000x reference)
.LBB0_23:
	s_and_b64 vcc, exec, s[4:5]
	s_cbranch_vccz .LBB0_358
	s_setprio 3
	s_load_dwordx4 s[12:15], s[0:1], 0x28
	s_load_dwordx2 s[4:5], s[0:1], 0x38
	s_load_dwordx2 s[24:25], s[0:1], 0x48
	s_lshl_b32 s3, s2, 2
	s_addk_i32 s3, 0xf7a8
	v_lshrrev_b32_e32 v1, 6, v0
	v_or_b32_e32 v2, s3, v1
	v_ashrrev_i32_e32 v3, 31, v2
	v_and_b32_e32 v7, 63, v0
	v_lshlrev_b64 v[4:5], 7, v[2:3]
	v_or_b32_e32 v4, v4, v7
	v_lshlrev_b64 v[12:13], 2, v[4:5]
	s_waitcnt lgkmcnt(0)
	v_lshl_add_u64 v[8:9], s[12:13], 0, v[12:13]
	global_load_dword v10, v[8:9], off nt
	global_load_dword v11, v[8:9], off offset:256 nt
	v_lshl_add_u64 v[14:15], s[14:15], 0, v[12:13]
	v_lshl_add_u64 v[12:13], s[4:5], 0, v[12:13]
	global_load_dword v9, v[14:15], off nt
	global_load_dword v8, v[14:15], off offset:256 nt
	global_load_dword v1, v[12:13], off nt
	global_load_dword v6, v[12:13], off offset:256 nt
	s_mov_b32 s3, 0xbfb8aa3b
	s_waitcnt vmcnt(5)
	v_add_f32_e32 v10, 0xc1200000, v10
	v_mul_f32_e64 v12, |v10|, s3
	v_exp_f32_e32 v13, v12
	s_mov_b32 s3, 0x3c23d70a
	v_cmp_ngt_f32_e32 vcc, s3, v13
	s_and_saveexec_b64 s[4:5], vcc
	s_xor_b64 s[10:11], exec, s[4:5]
	s_cbranch_execz .LBB0_26
	v_add_f32_e32 v12, 1.0, v13
	s_mov_b32 s3, 0x800000
	v_cmp_gt_f32_e32 vcc, s3, v12
	s_mov_b32 s3, 0x3f317217
	s_nop 0
	v_cndmask_b32_e64 v13, 0, 32, vcc
	v_ldexp_f32 v12, v12, v13
	v_log_f32_e32 v12, v12
	s_nop 0
	v_mul_f32_e32 v13, 0x3f317217, v12
	v_fma_f32 v13, v12, s3, -v13
	v_fmamk_f32 v13, v12, 0x3377d1cf, v13
	s_mov_b32 s3, 0x7f800000
	v_fmac_f32_e32 v13, 0x3f317217, v12
	v_cmp_lt_f32_e64 s[4:5], |v12|, s3
	s_nop 1
	v_cndmask_b32_e64 v12, v12, v13, s[4:5]
	v_mov_b32_e32 v13, 0x41b17218
	v_cndmask_b32_e32 v13, 0, v13, vcc
	v_sub_f32_e32 v12, v12, v13
